# dpp
# speedup vs baseline: 1.0074x; 1.0074x over previous
.LBB1_12:
	s_and_b32 s12, s19, 1
	s_lshr_b32 s13, s19, 1
	s_add_i32 s16, s19, 1
	v_lshl_add_u32 v231, s13, 3, v221
	s_cmp_lg_u32 s19, 3
	s_cselect_b32 s17, s16, 3
	s_waitcnt lgkmcnt(2)
	v_lshlrev_b32_e32 v2, 7, v231
	s_lshl_b32 s14, s12, 6
	v_or3_b32 v160, v2, s14, v220
	s_waitcnt lgkmcnt(0)
	v_mov_b32_e32 v1, v220
	v_lshl_add_u64 v[2:3], v[160:161], 2, s[6:7]
	global_load_dword v232, v[2:3], off
	s_lshl_b32 s14, s17, 2
	s_and_b32 s14, s14, 24
	s_lshl_b32 s13, s13, 9
	v_lshrrev_b32_e32 v3, 5, v1
	s_cmp_eq_u32 s12, 0
	v_add_u32_e32 v2, s14, v221
	v_lshlrev_b32_e32 v206, 4, v3
	s_cselect_b64 s[14:15], -1, 0
	s_cmp_eq_u32 s12, 1
	v_add3_u32 v149, v228, s13, v206
	s_cselect_b64 s[12:13], -1, 0
	s_lshl_b32 s17, s17, 6
	s_and_b32 s17, s17, 64
	v_lshl_or_b32 v2, v2, 7, s17
	v_lshl_add_u32 v234, v1, 4, 0
	v_and_or_b32 v1, v1, 31, v2
	v_mul_lo_u32 v2, v1, 27
	v_add_u32_e32 v233, 0xc000, v234
	v_mad_u64_u32 v[204:205], s[20:21], v3, 14, v[2:3]
	v_add_u32_e32 v202, 13, v2
	s_waitcnt vmcnt(3)
	v_mul_f32_e32 v1, 0.15915494, v222
	v_cos_f32_e32 v2, v1
	v_sin_f32_e32 v1, v1
	v_add_f32_e32 v2, v2, v2
	v_cndmask_b32_e64 v3, v2, v1, s[0:1]
	v_mul_f32_e32 v1, v1, v2
	v_fma_f32 v2, v2, v2, -2.0
	v_cndmask_b32_e64 v4, v2, v1, s[0:1]
	v_mul_f32_e32 v207, v1, v2
	v_fma_f32 v208, v2, v2, -2.0
	v_mul_f32_e32 v2, 0.15915494, v182
	v_cvt_pk_fp8_f32 v131, v225, v3
	v_cos_f32_e32 v3, v2
	v_sin_f32_e32 v2, v2
	v_cndmask_b32_e64 v1, v208, v207, s[0:1]
	v_cvt_pk_fp8_f32 v131, v4, v1 op_sel:[0,0,1]
	v_add_f32_e32 v1, v3, v3
	v_cvt_pk_f16_f32 v1, v2, v1
	v_cvt_pk_fp8_f32 v128, v182, v0
	v_cvt_scalef32_pk_fp8_f16 v132, v1, 1.0
	v_pk_fma_f16 v1, v1, v1, -2.0 op_sel:[1,0,1] op_sel_hi:[1,1,0]
	v_mul_f32_e32 v0, 0.15915494, v0
	v_cvt_scalef32_pk_fp8_f16 v132, v1, 1.0 op_sel:[0,0,1]
	v_pk_fma_f16 v1, v1, v1, -2.0 op_sel:[0,1,1] op_sel_hi:[1,1,0]
	v_cos_f32_e32 v2, v0
	v_cvt_scalef32_pk_fp8_f16 v133, v1, 1.0
	v_pk_fma_f16 v1, v1, v1, -2.0 op_sel:[0,1,1] op_sel_hi:[1,1,0]
	v_sin_f32_e32 v0, v0
	v_cvt_scalef32_pk_fp8_f16 v133, v1, 1.0 op_sel:[0,0,1]
	v_pk_fma_f16 v1, v1, v1, -2.0 op_sel:[0,1,1] op_sel_hi:[1,1,0]
	s_nop 0
	v_cvt_scalef32_pk_fp8_f16 v134, v1, 1.0
	v_pk_fma_f16 v1, v1, v1, -2.0 op_sel:[0,1,1] op_sel_hi:[1,1,0]
	s_nop 0
	v_cvt_scalef32_pk_fp8_f16 v134, v1, 1.0 op_sel:[0,0,1]
	v_add_f32_e32 v1, v2, v2
	v_cvt_pk_f16_f32 v0, v0, v1
	v_cvt_scalef32_pk_fp8_f16 v135, v0, 1.0
	v_pk_fma_f16 v24, v0, v0, -2.0 op_sel:[1,0,1] op_sel_hi:[1,1,0]
	s_waitcnt vmcnt(2)
	v_mul_f32_e32 v0, 0.15915494, v224
	v_cos_f32_e32 v1, v0
	v_sin_f32_e32 v0, v0
	v_add_f32_e32 v1, v1, v1
	v_cndmask_b32_e64 v2, v1, v0, s[0:1]
	v_mul_f32_e32 v0, v0, v1
	v_fma_f32 v1, v1, v1, -2.0
	v_cndmask_b32_e64 v3, v1, v0, s[0:1]
	v_mul_f32_e32 v209, v0, v1
	v_fma_f32 v210, v1, v1, -2.0
	v_mul_f32_e32 v1, 0.15915494, v190
	s_waitcnt vmcnt(1)
	v_cvt_pk_fp8_f32 v19, v223, v2
	v_cos_f32_e32 v2, v1
	v_sin_f32_e32 v1, v1
	v_cndmask_b32_e64 v0, v210, v209, s[0:1]
	v_cvt_pk_fp8_f32 v19, v3, v0 op_sel:[0,0,1]
	v_add_f32_e32 v0, v2, v2
	v_cvt_pk_f16_f32 v0, v1, v0
	v_cvt_scalef32_pk_fp8_f16 v20, v0, 1.0
	v_pk_fma_f16 v0, v0, v0, -2.0 op_sel:[1,0,1] op_sel_hi:[1,1,0]
	v_mul_f32_e32 v1, 0.15915494, v191
	v_cvt_scalef32_pk_fp8_f16 v135, v24, 1.0 op_sel:[0,0,1]
	v_cvt_scalef32_pk_fp8_f16 v20, v0, 1.0 op_sel:[0,0,1]
	v_pk_fma_f16 v0, v0, v0, -2.0 op_sel:[0,1,1] op_sel_hi:[1,1,0]
	v_cos_f32_e32 v2, v1
	v_pk_fma_f16 v24, v24, v24, -2.0 op_sel:[0,1,1] op_sel_hi:[1,1,0]
	v_cvt_scalef32_pk_fp8_f16 v21, v0, 1.0
	v_pk_fma_f16 v0, v0, v0, -2.0 op_sel:[0,1,1] op_sel_hi:[1,1,0]
	v_sin_f32_e32 v1, v1
	v_pk_fma_f16 v35, v24, v24, -2.0 op_sel:[0,1,1] op_sel_hi:[1,1,0]
	v_cvt_pk_fp8_f32 v128, v25, v185 op_sel:[0,0,1]
	v_cvt_scalef32_pk_fp8_f16 v21, v0, 1.0 op_sel:[0,0,1]
	v_pk_fma_f16 v0, v0, v0, -2.0 op_sel:[0,1,1] op_sel_hi:[1,1,0]
	v_pk_fma_f16 v36, v35, v35, -2.0 op_sel:[0,1,1] op_sel_hi:[1,1,0]
	v_mul_f32_e32 v25, 0.15915494, v25
	v_cvt_pk_fp8_f32 v129, v198, v162
	v_cvt_pk_fp8_f32 v130, v178, v200
	v_cvt_pk_fp8_f32 v16, v190, v191
	v_cvt_pk_fp8_f32 v17, v194, v195
	v_cvt_pk_fp8_f32 v18, v186, v187
	v_cvt_scalef32_pk_fp8_f16 v22, v0, 1.0
	v_pk_fma_f16 v0, v0, v0, -2.0 op_sel:[0,1,1] op_sel_hi:[1,1,0]
	v_pk_fma_f16 v37, v36, v36, -2.0 op_sel:[0,1,1] op_sel_hi:[1,1,0]
	v_cvt_scalef32_pk_fp8_f16 v137, v36, 1.0
	v_cos_f32_e32 v36, v25
	v_cvt_scalef32_pk_fp8_f16 v22, v0, 1.0 op_sel:[0,0,1]
	v_add_f32_e32 v0, v2, v2
	v_sin_f32_e32 v25, v25
	v_cvt_pk_f16_f32 v0, v1, v0
	v_mov_b32_e32 v160, v204
	v_cvt_scalef32_pk_fp8_f16 v23, v0, 1.0
	v_pk_fma_f16 v34, v0, v0, -2.0 op_sel:[1,0,1] op_sel_hi:[1,1,0]
	ds_read_b128 v[26:29], v234
	ds_read_b128 v[30:33], v234 offset:1024
	ds_read_b128 v[8:11], v234 offset:2048
	ds_read_b128 v[12:15], v234 offset:3072
	ds_read_b128 v[0:3], v234 offset:4096
	ds_read_b128 v[4:7], v234 offset:5120
	ds_read_b128 v[152:155], v234 offset:6144
	ds_read_b128 v[156:159], v234 offset:7168
	ds_read_b128 v[96:99], v149
	ds_read_b128 v[100:103], v149 offset:32
	ds_read_b128 v[104:107], v149 offset:64
	ds_read_b128 v[108:111], v149 offset:96
	v_cvt_pk_fp8_f32 v129, v163, v201 op_sel:[0,0,1]
	v_cvt_pk_fp8_f32 v130, v179, v181 op_sel:[0,0,1]
	v_cvt_pk_fp8_f32 v16, v192, v193 op_sel:[0,0,1]
	v_cvt_pk_fp8_f32 v17, v196, v197 op_sel:[0,0,1]
	v_cvt_pk_fp8_f32 v18, v188, v189 op_sel:[0,0,1]
	v_cvt_scalef32_pk_fp8_f16 v136, v24, 1.0
	v_add_f32_e32 v24, v36, v36
	v_cvt_pk_f16_f32 v24, v25, v24
	v_pk_fma_f16 v25, v24, v24, -2.0 op_sel:[1,0,1] op_sel_hi:[1,1,0]
	v_cvt_scalef32_pk_fp8_f16 v138, v24, 1.0
	v_cvt_scalef32_pk_fp8_f16 v23, v34, 1.0 op_sel:[0,0,1]
	v_cvt_scalef32_pk_fp8_f16 v136, v35, 1.0 op_sel:[0,0,1]
	v_pk_fma_f16 v35, v25, v25, -2.0 op_sel:[0,1,1] op_sel_hi:[1,1,0]
	v_cvt_scalef32_pk_fp8_f16 v138, v25, 1.0 op_sel:[0,0,1]
	v_mul_f32_e32 v25, 0.15915494, v185
	s_waitcnt lgkmcnt(0)
	v_mfma_scale_f32_32x32x64_f8f6f4 v[112:127], v[26:33], v[16:23], v[96:111], v227, v226 op_sel_hi:[0,0,0]
	v_cvt_scalef32_pk_fp8_f16 v139, v35, 1.0
	v_pk_fma_f16 v35, v35, v35, -2.0 op_sel:[0,1,1] op_sel_hi:[1,1,0]
	s_nop 0
	v_pk_fma_f16 v24, v35, v35, -2.0 op_sel:[0,1,1] op_sel_hi:[1,1,0]
	ds_read_b128 v[64:67], v149 offset:128
	ds_read_b128 v[68:71], v149 offset:160
	ds_read_b128 v[72:75], v149 offset:192
	ds_read_b128 v[76:79], v149 offset:224
	v_cvt_scalef32_pk_fp8_f16 v140, v24, 1.0
	v_pk_fma_f16 v24, v24, v24, -2.0 op_sel:[0,1,1] op_sel_hi:[1,1,0]
	v_cvt_scalef32_pk_fp8_f16 v137, v37, 1.0 op_sel:[0,0,1]
	v_cvt_scalef32_pk_fp8_f16 v140, v24, 1.0 op_sel:[0,0,1]
	v_cvt_scalef32_pk_fp8_f16 v139, v35, 1.0 op_sel:[0,0,1]
	v_mfma_scale_f32_32x32x64_f8f6f4 v[96:111], v[26:33], v[128:135], v[96:111], v227, v226 op_sel_hi:[0,0,0]
	v_cos_f32_e32 v26, v25
	v_sin_f32_e32 v25, v25
	v_mul_f32_e32 v30, 0.15915494, v192
	v_mul_f32_e32 v31, 0.15915494, v193
	v_add_f32_e32 v24, v26, v26
	v_cvt_pk_f16_f32 v24, v25, v24
	v_cvt_scalef32_pk_fp8_f16 v141, v24, 1.0
	v_pk_fma_f16 v24, v24, v24, -2.0 op_sel:[1,0,1] op_sel_hi:[1,1,0]
	s_nop 0
	v_cvt_scalef32_pk_fp8_f16 v141, v24, 1.0 op_sel:[0,0,1]
	v_pk_fma_f16 v26, v24, v24, -2.0 op_sel:[0,1,1] op_sel_hi:[1,1,0]
	v_lshl_add_u64 v[24:25], v[160:161], 2, s[4:5]
	v_pk_fma_f16 v27, v26, v26, -2.0 op_sel:[0,1,1] op_sel_hi:[1,1,0]
	s_nop 0
	v_pk_fma_f16 v28, v27, v27, -2.0 op_sel:[0,1,1] op_sel_hi:[1,1,0]
	s_waitcnt lgkmcnt(0)
	v_mfma_scale_f32_32x32x64_f8f6f4 v[80:95], v[8:15], v[16:23], v[64:79], v227, v226 op_sel_hi:[0,0,0]
	global_load_dwordx4 v[182:185], v[24:25], off
	global_load_dwordx4 v[190:193], v[24:25], off offset:3456
	v_cos_f32_e32 v25, v31
	v_pk_fma_f16 v29, v28, v28, -2.0 op_sel:[0,1,1] op_sel_hi:[1,1,0]
	v_cvt_scalef32_pk_fp8_f16 v143, v28, 1.0
	v_cvt_scalef32_pk_fp8_f16 v142, v26, 1.0
	v_cvt_scalef32_pk_fp8_f16 v143, v29, 1.0 op_sel:[0,0,1]
	v_cvt_scalef32_pk_fp8_f16 v142, v27, 1.0 op_sel:[0,0,1]
	v_add_f32_e32 v150, v25, v25
	v_mfma_scale_f32_32x32x64_f8f6f4 v[64:79], v[8:15], v[128:135], v[64:79], v227, v226 op_sel_hi:[0,0,0]
	v_pk_fma_f16 v8, v34, v34, -2.0 op_sel:[0,1,1] op_sel_hi:[1,1,0]
	ds_read_b128 v[32:35], v149 offset:256
	ds_read_b128 v[36:39], v149 offset:288
	ds_read_b128 v[40:43], v149 offset:320
	ds_read_b128 v[44:47], v149 offset:352
	v_pk_fma_f16 v9, v8, v8, -2.0 op_sel:[0,1,1] op_sel_hi:[1,1,0]
	v_cvt_scalef32_pk_fp8_f16 v144, v8, 1.0
	v_pk_fma_f16 v10, v9, v9, -2.0 op_sel:[0,1,1] op_sel_hi:[1,1,0]
	v_cvt_scalef32_pk_fp8_f16 v144, v9, 1.0 op_sel:[0,0,1]
	v_pk_fma_f16 v11, v10, v10, -2.0 op_sel:[0,1,1] op_sel_hi:[1,1,0]
	v_cvt_scalef32_pk_fp8_f16 v145, v10, 1.0
	v_cos_f32_e32 v10, v30
	v_cvt_scalef32_pk_fp8_f16 v145, v11, 1.0 op_sel:[0,0,1]
	v_sin_f32_e32 v11, v30
	v_add_f32_e32 v8, v10, v10
	v_cvt_pk_f16_f32 v8, v11, v8
	v_pk_fma_f16 v9, v8, v8, -2.0 op_sel:[1,0,1] op_sel_hi:[1,1,0]
	v_cvt_scalef32_pk_fp8_f16 v146, v8, 1.0
	v_pk_fma_f16 v10, v9, v9, -2.0 op_sel:[0,1,1] op_sel_hi:[1,1,0]
	s_waitcnt lgkmcnt(0)
	v_mfma_scale_f32_32x32x64_f8f6f4 v[48:63], v[0:7], v[16:23], v[32:47], v227, v226 op_sel_hi:[0,0,0]
	v_cvt_scalef32_pk_fp8_f16 v147, v10, 1.0
	v_pk_fma_f16 v10, v10, v10, -2.0 op_sel:[0,1,1] op_sel_hi:[1,1,0]
	v_cvt_scalef32_pk_fp8_f16 v146, v9, 1.0 op_sel:[0,0,1]
	v_cvt_scalef32_pk_fp8_f16 v147, v10, 1.0 op_sel:[0,0,1]
	v_pk_fma_f16 v24, v10, v10, -2.0 op_sel:[0,1,1] op_sel_hi:[1,1,0]
	s_nop 0
	v_cvt_scalef32_pk_fp8_f16 v148, v24, 1.0
	v_pk_fma_f16 v24, v24, v24, -2.0 op_sel:[0,1,1] op_sel_hi:[1,1,0]
	s_nop 0
	v_cvt_scalef32_pk_fp8_f16 v148, v24, 1.0 op_sel:[0,0,1]
	v_mfma_scale_f32_32x32x64_f8f6f4 v[32:47], v[0:7], v[128:135], v[32:47], v227, v226 op_sel_hi:[0,0,0]
	ds_read_b128 v[0:3], v149 offset:384
	ds_read_b128 v[4:7], v149 offset:416
	ds_read_b128 v[8:11], v149 offset:448
	ds_read_b128 v[12:15], v149 offset:480
	v_sin_f32_e32 v149, v31
	s_nop 0
	v_cvt_pk_f16_f32 v150, v149, v150
	v_cvt_scalef32_pk_fp8_f16 v149, v150, 1.0
	v_pk_fma_f16 v150, v150, v150, -2.0 op_sel:[1,0,1] op_sel_hi:[1,1,0]
	s_nop 0
	v_pk_fma_f16 v160, v150, v150, -2.0 op_sel:[0,1,1] op_sel_hi:[1,1,0]
	v_cvt_scalef32_pk_fp8_f16 v149, v150, 1.0 op_sel:[0,0,1]
	v_pk_fma_f16 v164, v160, v160, -2.0 op_sel:[0,1,1] op_sel_hi:[1,1,0]
	s_nop 0
	v_pk_fma_f16 v150, v164, v164, -2.0 op_sel:[0,1,1] op_sel_hi:[1,1,0]
	s_waitcnt lgkmcnt(0)
	v_mfma_scale_f32_32x32x64_f8f6f4 v[16:31], v[152:159], v[16:23], v[0:15], v227, v226 op_sel_hi:[0,0,0]
	v_pk_fma_f16 v165, v150, v150, -2.0 op_sel:[0,1,1] op_sel_hi:[1,1,0]
	v_cvt_scalef32_pk_fp8_f16 v151, v150, 1.0
	v_cvt_scalef32_pk_fp8_f16 v150, v160, 1.0
	v_cvt_scalef32_pk_fp8_f16 v151, v165, 1.0 op_sel:[0,0,1]
	v_cvt_scalef32_pk_fp8_f16 v150, v164, 1.0 op_sel:[0,0,1]
	v_mfma_scale_f32_32x32x64_f8f6f4 v[0:15], v[152:159], v[128:135], v[0:15], v227, v226 op_sel_hi:[0,0,0]
	v_mul_f32_e32 v128, 0.15915494, v198
	v_cos_f32_e32 v129, v128
	v_sin_f32_e32 v128, v128
	v_mul_f32_e32 v133, 0.15915494, v162
	v_cos_f32_e32 v134, v133
	v_add_f32_e32 v129, v129, v129
	v_cvt_pk_f16_f32 v130, v128, v129
	v_pk_fma_f16 v131, v130, v130, -2.0 op_sel:[1,0,1] op_sel_hi:[1,1,0]
	v_sin_f32_e32 v133, v133
	v_pk_fma_f16 v128, v131, v131, -2.0 op_sel:[0,1,1] op_sel_hi:[1,1,0]
	s_nop 0
	v_pk_fma_f16 v132, v128, v128, -2.0 op_sel:[0,1,1] op_sel_hi:[1,1,0]
	v_cvt_scalef32_pk_fp8_f16 v129, v128, 1.0
	v_cvt_scalef32_pk_fp8_f16 v128, v130, 1.0
	v_add_f32_e32 v130, v134, v134
	v_cvt_scalef32_pk_fp8_f16 v128, v131, 1.0 op_sel:[0,0,1]
	v_cvt_pk_f16_f32 v130, v133, v130
	v_cvt_scalef32_pk_fp8_f16 v129, v132, 1.0 op_sel:[0,0,1]
	v_cvt_scalef32_pk_fp8_f16 v131, v130, 1.0
	v_pk_fma_f16 v133, v130, v130, -2.0 op_sel:[1,0,1] op_sel_hi:[1,1,0]
	v_pk_fma_f16 v132, v132, v132, -2.0 op_sel:[0,1,1] op_sel_hi:[1,1,0]
	ds_read_b128 v[152:155], v234 offset:8192
	ds_read_b128 v[156:159], v234 offset:9216
	ds_read_b128 v[164:167], v234 offset:10240
	ds_read_b128 v[168:171], v234 offset:11264
	ds_read_b128 v[236:239], v234 offset:12288
	ds_read_b128 v[240:243], v234 offset:13312
	v_cvt_scalef32_pk_fp8_f16 v130, v132, 1.0
	v_pk_fma_f16 v132, v132, v132, -2.0 op_sel:[0,1,1] op_sel_hi:[1,1,0]
	v_mul_f32_e32 v135, 0.15915494, v163
	s_waitcnt lgkmcnt(4)
	v_mfma_scale_f32_32x32x64_f8f6f4 v[96:111], v[152:159], v[136:143], v[96:111], v227, v226 op_sel_hi:[0,0,0]
	v_cvt_scalef32_pk_fp8_f16 v131, v133, 1.0 op_sel:[0,0,1]
	v_pk_fma_f16 v133, v133, v133, -2.0 op_sel:[0,1,1] op_sel_hi:[1,1,0]
	v_cvt_scalef32_pk_fp8_f16 v130, v132, 1.0 op_sel:[0,0,1]
	v_cvt_scalef32_pk_fp8_f16 v132, v133, 1.0
	v_pk_fma_f16 v133, v133, v133, -2.0 op_sel:[0,1,1] op_sel_hi:[1,1,0]
	ds_read_b128 v[244:247], v234 offset:14336
	ds_read_b128 v[248:251], v234 offset:15360
	v_pk_fma_f16 v134, v133, v133, -2.0 op_sel:[0,1,1] op_sel_hi:[1,1,0]
	v_cvt_scalef32_pk_fp8_f16 v132, v133, 1.0 op_sel:[0,0,1]
	v_cvt_scalef32_pk_fp8_f16 v133, v134, 1.0
	v_pk_fma_f16 v134, v134, v134, -2.0 op_sel:[0,1,1] op_sel_hi:[1,1,0]
	s_nop 0
	v_cvt_scalef32_pk_fp8_f16 v133, v134, 1.0 op_sel:[0,0,1]
	v_mfma_scale_f32_32x32x64_f8f6f4 v[112:127], v[152:159], v[144:151], v[112:127], v227, v226 op_sel_hi:[0,0,0]
	v_cos_f32_e32 v152, v135
	v_sin_f32_e32 v135, v135
	v_mul_f32_e32 v154, 0.15915494, v194
	v_cos_f32_e32 v155, v154
	v_add_f32_e32 v134, v152, v152
	v_cvt_pk_f16_f32 v152, v135, v134
	v_pk_fma_f16 v153, v152, v152, -2.0 op_sel:[1,0,1] op_sel_hi:[1,1,0]
	v_sin_f32_e32 v154, v154
	v_pk_fma_f16 v134, v153, v153, -2.0 op_sel:[0,1,1] op_sel_hi:[1,1,0]
	s_nop 0
	v_pk_fma_f16 v160, v134, v134, -2.0 op_sel:[0,1,1] op_sel_hi:[1,1,0]
	v_cvt_scalef32_pk_fp8_f16 v135, v134, 1.0
	v_cvt_scalef32_pk_fp8_f16 v134, v152, 1.0
	v_add_f32_e32 v152, v155, v155
	s_waitcnt lgkmcnt(4)
	v_mfma_scale_f32_32x32x64_f8f6f4 v[64:79], v[164:171], v[136:143], v[64:79], v227, v226 op_sel_hi:[0,0,0]
	v_mul_f32_e32 v157, 0.15915494, v195
	v_cvt_pk_f16_f32 v154, v154, v152
	v_cos_f32_e32 v158, v157
	v_pk_fma_f16 v155, v154, v154, -2.0 op_sel:[1,0,1] op_sel_hi:[1,1,0]
	v_sin_f32_e32 v157, v157
	v_pk_fma_f16 v152, v155, v155, -2.0 op_sel:[0,1,1] op_sel_hi:[1,1,0]
	v_cvt_scalef32_pk_fp8_f16 v134, v153, 1.0 op_sel:[0,0,1]
	v_pk_fma_f16 v156, v152, v152, -2.0 op_sel:[0,1,1] op_sel_hi:[1,1,0]
	v_cvt_scalef32_pk_fp8_f16 v153, v152, 1.0
	v_cvt_scalef32_pk_fp8_f16 v152, v154, 1.0
	v_add_f32_e32 v154, v158, v158
	v_mul_f32_e32 v159, 0.15915494, v196
	v_cvt_scalef32_pk_fp8_f16 v152, v155, 1.0 op_sel:[0,0,1]
	v_mfma_scale_f32_32x32x64_f8f6f4 v[80:95], v[164:171], v[144:151], v[80:95], v227, v226 op_sel_hi:[0,0,0]
	v_cvt_pk_f16_f32 v154, v157, v154
	v_cvt_scalef32_pk_fp8_f16 v153, v156, 1.0 op_sel:[0,0,1]
	v_cvt_scalef32_pk_fp8_f16 v155, v154, 1.0
	v_pk_fma_f16 v156, v156, v156, -2.0 op_sel:[0,1,1] op_sel_hi:[1,1,0]
	v_pk_fma_f16 v157, v154, v154, -2.0 op_sel:[1,0,1] op_sel_hi:[1,1,0]
	v_cvt_scalef32_pk_fp8_f16 v154, v156, 1.0
	v_pk_fma_f16 v156, v156, v156, -2.0 op_sel:[0,1,1] op_sel_hi:[1,1,0]
	v_cvt_scalef32_pk_fp8_f16 v155, v157, 1.0 op_sel:[0,0,1]
	v_pk_fma_f16 v157, v157, v157, -2.0 op_sel:[0,1,1] op_sel_hi:[1,1,0]
	v_cvt_scalef32_pk_fp8_f16 v154, v156, 1.0 op_sel:[0,0,1]
	v_cvt_scalef32_pk_fp8_f16 v156, v157, 1.0
	v_pk_fma_f16 v157, v157, v157, -2.0 op_sel:[0,1,1] op_sel_hi:[1,1,0]
	s_waitcnt lgkmcnt(0)
	v_mfma_scale_f32_32x32x64_f8f6f4 v[0:15], v[244:251], v[136:143], v[0:15], v227, v226 op_sel_hi:[0,0,0]
	v_cvt_scalef32_pk_fp8_f16 v156, v157, 1.0 op_sel:[0,0,1]
	v_pk_fma_f16 v158, v157, v157, -2.0 op_sel:[0,1,1] op_sel_hi:[1,1,0]
	v_cvt_scalef32_pk_fp8_f16 v135, v160, 1.0 op_sel:[0,0,1]
	v_cvt_scalef32_pk_fp8_f16 v157, v158, 1.0
	v_mfma_scale_f32_32x32x64_f8f6f4 v[32:47], v[236:243], v[136:143], v[32:47], v227, v226 op_sel_hi:[0,0,0]
	v_cos_f32_e32 v136, v159
	v_sin_f32_e32 v137, v159
	v_pk_fma_f16 v138, v158, v158, -2.0 op_sel:[0,1,1] op_sel_hi:[1,1,0]
	v_add_f32_e32 v136, v136, v136
	v_cvt_pk_f16_f32 v136, v137, v136
	v_pk_fma_f16 v137, v136, v136, -2.0 op_sel:[1,0,1] op_sel_hi:[1,1,0]
	v_cvt_scalef32_pk_fp8_f16 v157, v138, 1.0 op_sel:[0,0,1]
	v_pk_fma_f16 v138, v137, v137, -2.0 op_sel:[0,1,1] op_sel_hi:[1,1,0]
	s_nop 0
	v_pk_fma_f16 v180, v138, v138, -2.0 op_sel:[0,1,1] op_sel_hi:[1,1,0]
	v_cvt_scalef32_pk_fp8_f16 v159, v138, 1.0
	v_cvt_scalef32_pk_fp8_f16 v158, v136, 1.0
	v_cvt_scalef32_pk_fp8_f16 v159, v180, 1.0 op_sel:[0,0,1]
	v_cvt_scalef32_pk_fp8_f16 v158, v137, 1.0 op_sel:[0,0,1]
	v_mfma_scale_f32_32x32x64_f8f6f4 v[48:63], v[236:243], v[144:151], v[48:63], v227, v226 op_sel_hi:[0,0,0]
	v_mfma_scale_f32_32x32x64_f8f6f4 v[16:31], v[244:251], v[144:151], v[16:31], v227, v226 op_sel_hi:[0,0,0]
	ds_read_b128 v[140:143], v234 offset:16384
	ds_read_b128 v[144:147], v234 offset:17408
	ds_read_b128 v[236:239], v234 offset:18432
	ds_read_b128 v[240:243], v234 offset:19456
	ds_read_b128 v[170:173], v234 offset:20480
	ds_read_b128 v[174:177], v234 offset:21504
	s_waitcnt lgkmcnt(4)
	v_mfma_scale_f32_32x32x64_f8f6f4 v[96:111], v[140:147], v[128:135], v[96:111], v227, v226 op_sel_hi:[0,0,0]
	v_pk_fma_f16 v139, v160, v160, -2.0 op_sel:[0,1,1] op_sel_hi:[1,1,0]
	v_mov_b32_e32 v160, v204
	ds_read_b128 v[162:165], v234 offset:22528
	ds_read_b128 v[166:169], v234 offset:23552
	v_mul_f32_e32 v136, 0.15915494, v201
	v_cos_f32_e32 v137, v136
	v_sin_f32_e32 v136, v136
	v_mul_f32_e32 v150, 0.15915494, v186
	v_cos_f32_e32 v151, v150
	v_add_f32_e32 v137, v137, v137
	v_cvt_pk_f16_f32 v136, v136, v137
	v_pk_fma_f16 v138, v136, v136, -2.0 op_sel:[1,0,1] op_sel_hi:[1,1,0]
	v_cvt_scalef32_pk_fp8_f16 v137, v136, 1.0
	v_mfma_scale_f32_32x32x64_f8f6f4 v[112:127], v[140:147], v[152:159], v[112:127], v227, v226 op_sel_hi:[0,0,0]
	v_mul_f32_e32 v140, 0.15915494, v178
	v_cos_f32_e32 v141, v140
	v_sin_f32_e32 v140, v140
	v_mul_f32_e32 v143, 0.15915494, v200
	v_cos_f32_e32 v144, v143
	v_add_f32_e32 v141, v141, v141
	v_cvt_pk_f16_f32 v141, v140, v141
	v_sin_f32_e32 v143, v143
	v_cvt_scalef32_pk_fp8_f16 v140, v141, 1.0
	v_pk_fma_f16 v141, v141, v141, -2.0 op_sel:[1,0,1] op_sel_hi:[1,1,0]
	v_mul_f32_e32 v146, 0.15915494, v197
	v_pk_fma_f16 v142, v141, v141, -2.0 op_sel:[0,1,1] op_sel_hi:[1,1,0]
	v_cvt_scalef32_pk_fp8_f16 v140, v141, 1.0 op_sel:[0,0,1]
	v_cvt_scalef32_pk_fp8_f16 v141, v142, 1.0
	v_pk_fma_f16 v145, v142, v142, -2.0 op_sel:[0,1,1] op_sel_hi:[1,1,0]
	v_add_f32_e32 v142, v144, v144
	v_cvt_pk_f16_f32 v144, v143, v142
	v_lshl_add_u64 v[142:143], v[160:161], 2, s[4:5]
	global_load_dwordx4 v[198:201], v[142:143], off offset:16
	global_load_dwordx4 v[194:197], v[142:143], off offset:3472
	v_cvt_scalef32_pk_fp8_f16 v141, v145, 1.0 op_sel:[0,0,1]
	v_pk_fma_f16 v160, v144, v144, -2.0 op_sel:[1,0,1] op_sel_hi:[1,1,0]
	v_cvt_scalef32_pk_fp8_f16 v143, v144, 1.0
	v_pk_fma_f16 v144, v145, v145, -2.0 op_sel:[0,1,1] op_sel_hi:[1,1,0]
	v_cos_f32_e32 v145, v146
	v_sin_f32_e32 v146, v146
	v_pk_fma_f16 v148, v138, v138, -2.0 op_sel:[0,1,1] op_sel_hi:[1,1,0]
	v_cvt_scalef32_pk_fp8_f16 v136, v139, 1.0
	v_pk_fma_f16 v139, v139, v139, -2.0 op_sel:[0,1,1] op_sel_hi:[1,1,0]
	v_pk_fma_f16 v149, v148, v148, -2.0 op_sel:[0,1,1] op_sel_hi:[1,1,0]
	v_cvt_scalef32_pk_fp8_f16 v142, v144, 1.0
	v_pk_fma_f16 v144, v144, v144, -2.0 op_sel:[0,1,1] op_sel_hi:[1,1,0]
	v_cvt_scalef32_pk_fp8_f16 v137, v138, 1.0 op_sel:[0,0,1]
	v_cvt_scalef32_pk_fp8_f16 v136, v139, 1.0 op_sel:[0,0,1]
	v_pk_fma_f16 v138, v149, v149, -2.0 op_sel:[0,1,1] op_sel_hi:[1,1,0]
	v_cvt_scalef32_pk_fp8_f16 v142, v144, 1.0 op_sel:[0,0,1]
	v_add_f32_e32 v144, v145, v145
	v_cvt_scalef32_pk_fp8_f16 v139, v138, 1.0
	v_pk_fma_f16 v138, v138, v138, -2.0 op_sel:[0,1,1] op_sel_hi:[1,1,0]
	s_waitcnt lgkmcnt(4)
	v_mfma_scale_f32_32x32x64_f8f6f4 v[64:79], v[236:243], v[128:135], v[64:79], v227, v226 op_sel_hi:[0,0,0]
	v_cvt_pk_f16_f32 v144, v146, v144
	v_cvt_scalef32_pk_fp8_f16 v139, v138, 1.0 op_sel:[0,0,1]
	v_pk_fma_f16 v146, v144, v144, -2.0 op_sel:[1,0,1] op_sel_hi:[1,1,0]
	v_cvt_scalef32_pk_fp8_f16 v138, v148, 1.0
	v_cvt_scalef32_pk_fp8_f16 v145, v144, 1.0
	v_pk_fma_f16 v147, v180, v180, -2.0 op_sel:[0,1,1] op_sel_hi:[1,1,0]
	v_pk_fma_f16 v148, v146, v146, -2.0 op_sel:[0,1,1] op_sel_hi:[1,1,0]
	v_cvt_scalef32_pk_fp8_f16 v138, v149, 1.0 op_sel:[0,0,1]
	v_cvt_scalef32_pk_fp8_f16 v144, v147, 1.0
	v_pk_fma_f16 v147, v147, v147, -2.0 op_sel:[0,1,1] op_sel_hi:[1,1,0]
	v_pk_fma_f16 v149, v148, v148, -2.0 op_sel:[0,1,1] op_sel_hi:[1,1,0]
	v_cvt_scalef32_pk_fp8_f16 v145, v146, 1.0 op_sel:[0,0,1]
	v_mfma_scale_f32_32x32x64_f8f6f4 v[80:95], v[236:243], v[152:159], v[80:95], v227, v226 op_sel_hi:[0,0,0]
	v_pk_fma_f16 v146, v149, v149, -2.0 op_sel:[0,1,1] op_sel_hi:[1,1,0]
	v_cvt_scalef32_pk_fp8_f16 v144, v147, 1.0 op_sel:[0,0,1]
	v_cvt_scalef32_pk_fp8_f16 v147, v146, 1.0
	v_pk_fma_f16 v146, v146, v146, -2.0 op_sel:[0,1,1] op_sel_hi:[1,1,0]
	v_sin_f32_e32 v150, v150
	v_cvt_scalef32_pk_fp8_f16 v147, v146, 1.0 op_sel:[0,0,1]
	v_cvt_scalef32_pk_fp8_f16 v146, v148, 1.0
	v_add_f32_e32 v148, v151, v151
	v_mul_f32_e32 v151, 0.15915494, v187
	v_cvt_scalef32_pk_fp8_f16 v146, v149, 1.0 op_sel:[0,0,1]
	v_cvt_pk_f16_f32 v149, v150, v148
	v_cvt_scalef32_pk_fp8_f16 v148, v149, 1.0
	s_waitcnt lgkmcnt(0)
	v_mfma_scale_f32_32x32x64_f8f6f4 v[0:15], v[162:169], v[128:135], v[0:15], v227, v226 op_sel_hi:[0,0,0]
	v_pk_fma_f16 v149, v149, v149, -2.0 op_sel:[1,0,1] op_sel_hi:[1,1,0]
	v_cvt_scalef32_pk_fp8_f16 v143, v160, 1.0 op_sel:[0,0,1]
	v_pk_fma_f16 v150, v149, v149, -2.0 op_sel:[0,1,1] op_sel_hi:[1,1,0]
	v_cvt_scalef32_pk_fp8_f16 v148, v149, 1.0 op_sel:[0,0,1]
	v_cvt_scalef32_pk_fp8_f16 v149, v150, 1.0
	v_mfma_scale_f32_32x32x64_f8f6f4 v[32:47], v[170:177], v[128:135], v[32:47], v227, v226 op_sel_hi:[0,0,0]
	v_cos_f32_e32 v128, v151
	v_sin_f32_e32 v129, v151
	v_pk_fma_f16 v130, v150, v150, -2.0 op_sel:[0,1,1] op_sel_hi:[1,1,0]
	v_add_f32_e32 v128, v128, v128
	v_cvt_pk_f16_f32 v128, v129, v128
	v_pk_fma_f16 v203, v128, v128, -2.0 op_sel:[1,0,1] op_sel_hi:[1,1,0]
	v_cvt_scalef32_pk_fp8_f16 v151, v128, 1.0
	v_pk_fma_f16 v128, v130, v130, -2.0 op_sel:[0,1,1] op_sel_hi:[1,1,0]
	s_nop 0
	v_cvt_scalef32_pk_fp8_f16 v150, v128, 1.0
	v_pk_fma_f16 v128, v128, v128, -2.0 op_sel:[0,1,1] op_sel_hi:[1,1,0]
	v_cvt_scalef32_pk_fp8_f16 v149, v130, 1.0 op_sel:[0,0,1]
	v_cvt_scalef32_pk_fp8_f16 v151, v203, 1.0 op_sel:[0,0,1]
	v_cvt_scalef32_pk_fp8_f16 v150, v128, 1.0 op_sel:[0,0,1]
	v_mfma_scale_f32_32x32x64_f8f6f4 v[48:63], v[170:177], v[152:159], v[48:63], v227, v226 op_sel_hi:[0,0,0]
	v_mfma_scale_f32_32x32x64_f8f6f4 v[16:31], v[162:169], v[152:159], v[16:31], v227, v226 op_sel_hi:[0,0,0]
	v_pk_fma_f16 v130, v160, v160, -2.0 op_sel:[0,1,1] op_sel_hi:[1,1,0]
	s_nop 0
	v_pk_fma_f16 v131, v130, v130, -2.0 op_sel:[0,1,1] op_sel_hi:[1,1,0]
	ds_read_b128 v[152:155], v234 offset:24576
	ds_read_b128 v[156:159], v234 offset:25600
	ds_read_b128 v[162:165], v234 offset:26624
	ds_read_b128 v[166:169], v234 offset:27648
	v_pk_fma_f16 v128, v131, v131, -2.0 op_sel:[0,1,1] op_sel_hi:[1,1,0]
	v_mov_b32_e32 v160, v204
	v_pk_fma_f16 v132, v128, v128, -2.0 op_sel:[0,1,1] op_sel_hi:[1,1,0]
	v_cvt_scalef32_pk_fp8_f16 v129, v128, 1.0
	v_cvt_scalef32_pk_fp8_f16 v129, v132, 1.0 op_sel:[0,0,1]
	v_mul_f32_e32 v132, 0.15915494, v179
	v_sin_f32_e32 v133, v132
	v_cos_f32_e32 v132, v132
	v_cvt_scalef32_pk_fp8_f16 v128, v130, 1.0
	v_cvt_scalef32_pk_fp8_f16 v128, v131, 1.0 op_sel:[0,0,1]
	v_add_f32_e32 v130, v132, v132
	v_cvt_pk_f16_f32 v132, v133, v130
	v_pk_fma_f16 v133, v132, v132, -2.0 op_sel:[1,0,1] op_sel_hi:[1,1,0]
	s_nop 0
	v_pk_fma_f16 v130, v133, v133, -2.0 op_sel:[0,1,1] op_sel_hi:[1,1,0]
	s_waitcnt lgkmcnt(2)
	v_mfma_scale_f32_32x32x64_f8f6f4 v[96:111], v[152:159], v[136:143], v[96:111], v227, v226 op_sel_hi:[0,0,0]
	v_cvt_scalef32_pk_fp8_f16 v131, v130, 1.0
	v_pk_fma_f16 v134, v130, v130, -2.0 op_sel:[0,1,1] op_sel_hi:[1,1,0]
	v_cvt_scalef32_pk_fp8_f16 v130, v132, 1.0
	v_cvt_scalef32_pk_fp8_f16 v131, v134, 1.0 op_sel:[0,0,1]
	v_cvt_scalef32_pk_fp8_f16 v130, v133, 1.0 op_sel:[0,0,1]
	v_pk_fma_f16 v133, v134, v134, -2.0 op_sel:[0,1,1] op_sel_hi:[1,1,0]
	v_mul_f32_e32 v134, 0.15915494, v181
	v_cos_f32_e32 v135, v134
	v_sin_f32_e32 v134, v134
	v_cvt_scalef32_pk_fp8_f16 v132, v133, 1.0
	v_pk_fma_f16 v133, v133, v133, -2.0 op_sel:[0,1,1] op_sel_hi:[1,1,0]
	ds_read_b128 v[170:173], v234 offset:28672
	ds_read_b128 v[174:177], v234 offset:29696
	ds_read_b128 v[236:239], v234 offset:30720
	ds_read_b128 v[240:243], v234 offset:31744
	v_cvt_scalef32_pk_fp8_f16 v132, v133, 1.0 op_sel:[0,0,1]
	v_add_f32_e32 v133, v135, v135
	v_mfma_scale_f32_32x32x64_f8f6f4 v[112:127], v[152:159], v[144:151], v[112:127], v227, v226 op_sel_hi:[0,0,0]
	v_cvt_pk_f16_f32 v152, v134, v133
	v_mul_f32_e32 v153, 0.15915494, v188
	v_lshl_add_u64 v[134:135], v[160:161], 2, s[4:5]
	v_mul_f32_e32 v154, 0.15915494, v189
	global_load_dwordx4 v[178:181], v[134:135], off offset:32
	global_load_dwordx4 v[186:189], v[134:135], off offset:3488
	v_pk_fma_f16 v134, v152, v152, -2.0 op_sel:[1,0,1] op_sel_hi:[1,1,0]
	v_cvt_scalef32_pk_fp8_f16 v133, v152, 1.0
	v_pk_fma_f16 v152, v134, v134, -2.0 op_sel:[0,1,1] op_sel_hi:[1,1,0]
	v_cvt_scalef32_pk_fp8_f16 v133, v134, 1.0 op_sel:[0,0,1]
	v_pk_fma_f16 v155, v152, v152, -2.0 op_sel:[0,1,1] op_sel_hi:[1,1,0]
	s_nop 0
	v_pk_fma_f16 v134, v155, v155, -2.0 op_sel:[0,1,1] op_sel_hi:[1,1,0]
	s_nop 0
	v_pk_fma_f16 v156, v134, v134, -2.0 op_sel:[0,1,1] op_sel_hi:[1,1,0]
	v_cvt_scalef32_pk_fp8_f16 v135, v134, 1.0
	v_cvt_scalef32_pk_fp8_f16 v134, v152, 1.0
	v_pk_fma_f16 v152, v203, v203, -2.0 op_sel:[0,1,1] op_sel_hi:[1,1,0]
	v_cvt_scalef32_pk_fp8_f16 v134, v155, 1.0 op_sel:[0,0,1]
	v_pk_fma_f16 v155, v152, v152, -2.0 op_sel:[0,1,1] op_sel_hi:[1,1,0]
	s_waitcnt lgkmcnt(4)
	v_mfma_scale_f32_32x32x64_f8f6f4 v[64:79], v[162:169], v[136:143], v[64:79], v227, v226 op_sel_hi:[0,0,0]
	v_cvt_scalef32_pk_fp8_f16 v135, v156, 1.0 op_sel:[0,0,1]
	v_pk_fma_f16 v156, v155, v155, -2.0 op_sel:[0,1,1] op_sel_hi:[1,1,0]
	s_nop 0
	v_pk_fma_f16 v157, v156, v156, -2.0 op_sel:[0,1,1] op_sel_hi:[1,1,0]
	v_mfma_scale_f32_32x32x64_f8f6f4 v[80:95], v[162:169], v[144:151], v[80:95], v227, v226 op_sel_hi:[0,0,0]
	v_cvt_scalef32_pk_fp8_f16 v165, v156, 1.0
	v_cos_f32_e32 v156, v153
	v_sin_f32_e32 v153, v153
	v_cvt_scalef32_pk_fp8_f16 v164, v152, 1.0
	v_add_f32_e32 v152, v156, v156
	v_cvt_pk_f16_f32 v152, v153, v152
	v_pk_fma_f16 v153, v152, v152, -2.0 op_sel:[1,0,1] op_sel_hi:[1,1,0]
	v_cvt_scalef32_pk_fp8_f16 v166, v152, 1.0
	v_cvt_scalef32_pk_fp8_f16 v164, v155, 1.0 op_sel:[0,0,1]
	v_pk_fma_f16 v155, v153, v153, -2.0 op_sel:[0,1,1] op_sel_hi:[1,1,0]
	v_cvt_scalef32_pk_fp8_f16 v166, v153, 1.0 op_sel:[0,0,1]
	s_waitcnt lgkmcnt(0)
	v_mfma_scale_f32_32x32x64_f8f6f4 v[0:15], v[236:243], v[136:143], v[0:15], v227, v226 op_sel_hi:[0,0,0]
	v_cos_f32_e32 v153, v154
	v_cvt_scalef32_pk_fp8_f16 v167, v155, 1.0
	v_pk_fma_f16 v155, v155, v155, -2.0 op_sel:[0,1,1] op_sel_hi:[1,1,0]
	v_sin_f32_e32 v154, v154
	v_pk_fma_f16 v152, v155, v155, -2.0 op_sel:[0,1,1] op_sel_hi:[1,1,0]
	s_nop 0
	v_cvt_scalef32_pk_fp8_f16 v168, v152, 1.0
	v_pk_fma_f16 v152, v152, v152, -2.0 op_sel:[0,1,1] op_sel_hi:[1,1,0]
	s_nop 0
	v_cvt_scalef32_pk_fp8_f16 v168, v152, 1.0 op_sel:[0,0,1]
	v_add_f32_e32 v152, v153, v153
	v_cvt_scalef32_pk_fp8_f16 v165, v157, 1.0 op_sel:[0,0,1]
	v_cvt_scalef32_pk_fp8_f16 v167, v155, 1.0 op_sel:[0,0,1]
	v_mfma_scale_f32_32x32x64_f8f6f4 v[32:47], v[170:177], v[136:143], v[32:47], v227, v226 op_sel_hi:[0,0,0]
	v_cvt_pk_f16_f32 v136, v154, v152
	v_cvt_scalef32_pk_fp8_f16 v169, v136, 1.0
	v_pk_fma_f16 v136, v136, v136, -2.0 op_sel:[1,0,1] op_sel_hi:[1,1,0]
	s_nop 0
	v_cvt_scalef32_pk_fp8_f16 v169, v136, 1.0 op_sel:[0,0,1]
	v_pk_fma_f16 v136, v136, v136, -2.0 op_sel:[0,1,1] op_sel_hi:[1,1,0]
	s_nop 0
	v_pk_fma_f16 v137, v136, v136, -2.0 op_sel:[0,1,1] op_sel_hi:[1,1,0]
	s_nop 0
	v_pk_fma_f16 v138, v137, v137, -2.0 op_sel:[0,1,1] op_sel_hi:[1,1,0]
	s_nop 0
	v_pk_fma_f16 v139, v138, v138, -2.0 op_sel:[0,1,1] op_sel_hi:[1,1,0]
	v_mfma_scale_f32_32x32x64_f8f6f4 v[48:63], v[170:177], v[144:151], v[48:63], v227, v226 op_sel_hi:[0,0,0]
	v_cvt_scalef32_pk_fp8_f16 v171, v138, 1.0
	v_cvt_scalef32_pk_fp8_f16 v170, v136, 1.0
	v_cvt_scalef32_pk_fp8_f16 v171, v139, 1.0 op_sel:[0,0,1]
	v_cvt_scalef32_pk_fp8_f16 v170, v137, 1.0 op_sel:[0,0,1]
	v_mfma_scale_f32_32x32x64_f8f6f4 v[16:31], v[236:243], v[144:151], v[16:31], v227, v226 op_sel_hi:[0,0,0]
	v_mul_f32_e32 v152, 0.15915494, v225
	ds_read_b128 v[136:139], v234 offset:32768
	ds_read_b128 v[140:143], v234 offset:33792
	v_cos_f32_e32 v153, v152
	v_sin_f32_e32 v152, v152
	v_mov_b32_e32 v205, v161
	s_waitcnt lgkmcnt(0)
	v_mfma_scale_f32_32x32x64_f8f6f4 v[96:111], v[136:143], v[128:135], v[96:111], v227, v226 op_sel_hi:[0,0,0]
	v_add_f32_e32 v153, v153, v153
	v_cvt_pk_f16_f32 v158, v152, v153
	v_mov_b32_e32 v203, v161
	v_cndmask_b32_e64 v162, 0, v222, s[0:1]
	v_mul_f32_e32 v163, 0.15915494, v223
	v_pk_fma_f16 v159, v158, v158, -2.0 op_sel:[1,0,1] op_sel_hi:[1,1,0]
	v_cndmask_b32_e64 v172, 0, v224, s[0:1]
	v_pk_fma_f16 v156, v159, v159, -2.0 op_sel:[0,1,1] op_sel_hi:[1,1,0]
	s_nop 0
	v_pk_fma_f16 v160, v156, v156, -2.0 op_sel:[0,1,1] op_sel_hi:[1,1,0]
	v_cvt_scalef32_pk_fp8_f16 v157, v156, 1.0
	v_cvt_scalef32_pk_fp8_f16 v156, v158, 1.0
	v_cvt_scalef32_pk_fp8_f16 v156, v159, 1.0 op_sel:[0,0,1]
	v_mfma_scale_f32_32x32x64_f8f6f4 v[112:127], v[136:143], v[164:171], v[112:127], v227, v226 op_sel_hi:[0,0,0]
	ds_read_b128 v[136:139], v234 offset:34816
	ds_read_b128 v[140:143], v234 offset:35840
	ds_read_b128 v[144:147], v234 offset:36864
	ds_read_b128 v[148:151], v234 offset:37888
	ds_read_b128 v[236:239], v234 offset:38912
	ds_read_b128 v[240:243], v234 offset:39936
	v_lshl_add_u64 v[152:153], v[204:205], 2, s[4:5]
	v_lshl_add_u64 v[154:155], v[202:203], 2, s[4:5]
	global_load_dword v225, v[152:153], off offset:48
	global_load_dword v222, v[154:155], off
	global_load_dword v224, v[154:155], off offset:3456
	global_load_dword v223, v[152:153], off offset:3504
	v_cvt_scalef32_pk_fp8_f16 v157, v160, 1.0 op_sel:[0,0,1]
	s_waitcnt lgkmcnt(4)
	v_mfma_scale_f32_32x32x64_f8f6f4 v[64:79], v[136:143], v[128:135], v[64:79], v227, v226 op_sel_hi:[0,0,0]
	v_mfma_scale_f32_32x32x64_f8f6f4 v[80:95], v[136:143], v[164:171], v[80:95], v227, v226 op_sel_hi:[0,0,0]
	v_mul_f32_e32 v136, v207, v208
	v_fma_f32 v137, v208, v208, -2.0
	v_cndmask_b32_e64 v138, v137, v136, s[0:1]
	v_mul_f32_e32 v136, v136, v137
	v_fma_f32 v137, v137, v137, -2.0
	v_cndmask_b32_e64 v139, v137, v136, s[0:1]
	v_cvt_pk_fp8_f32 v159, v138, v139
	v_mul_f32_e32 v136, v136, v137
	v_fma_f32 v137, v137, v137, -2.0
	v_cndmask_b32_e64 v136, v137, v136, s[0:1]
	v_cvt_pk_fp8_f32 v159, v136, v162 op_sel:[0,0,1]
	v_pk_fma_f16 v136, v160, v160, -2.0 op_sel:[0,1,1] op_sel_hi:[1,1,0]
	v_mov_b32_e32 v160, v161
	v_pk_fma_f16 v137, v136, v136, -2.0 op_sel:[0,1,1] op_sel_hi:[1,1,0]
	v_cvt_scalef32_pk_fp8_f16 v158, v136, 1.0
	v_cos_f32_e32 v136, v163
	v_cvt_scalef32_pk_fp8_f16 v158, v137, 1.0 op_sel:[0,0,1]
	v_sin_f32_e32 v137, v163
	s_waitcnt lgkmcnt(0)
	v_mfma_scale_f32_32x32x64_f8f6f4 v[0:15], v[236:243], v[128:135], v[0:15], v227, v226 op_sel_hi:[0,0,0]
	v_add_f32_e32 v136, v136, v136
	v_mov_b32_e32 v162, v161
	v_cvt_pk_f16_f32 v138, v137, v136
	v_pk_fma_f16 v139, v138, v138, -2.0 op_sel:[1,0,1] op_sel_hi:[1,1,0]
	s_nop 0
	v_pk_fma_f16 v136, v139, v139, -2.0 op_sel:[0,1,1] op_sel_hi:[1,1,0]
	v_mov_b32_e32 v163, v161
	v_pk_fma_f16 v140, v136, v136, -2.0 op_sel:[0,1,1] op_sel_hi:[1,1,0]
	v_cvt_scalef32_pk_fp8_f16 v137, v136, 1.0
	v_cvt_scalef32_pk_fp8_f16 v136, v138, 1.0
	v_cvt_scalef32_pk_fp8_f16 v136, v139, 1.0 op_sel:[0,0,1]
	v_mul_f32_e32 v138, v209, v210
	v_fma_f32 v139, v210, v210, -2.0
	v_cndmask_b32_e64 v141, v139, v138, s[0:1]
	v_mul_f32_e32 v138, v138, v139
	v_fma_f32 v142, v139, v139, -2.0
	v_cndmask_b32_e64 v143, v142, v138, s[0:1]
	v_cvt_pk_fp8_f32 v139, v141, v143
	v_mfma_scale_f32_32x32x64_f8f6f4 v[32:47], v[144:151], v[128:135], v[32:47], v227, v226 op_sel_hi:[0,0,0]
	v_mul_f32_e32 v128, v138, v142
	v_fma_f32 v129, v142, v142, -2.0
	v_cndmask_b32_e64 v128, v129, v128, s[0:1]
	v_cvt_pk_fp8_f32 v139, v128, v172 op_sel:[0,0,1]
	v_pk_fma_f16 v128, v140, v140, -2.0 op_sel:[0,1,1] op_sel_hi:[1,1,0]
	s_nop 0
	v_cvt_scalef32_pk_fp8_f16 v138, v128, 1.0
	v_pk_fma_f16 v128, v128, v128, -2.0 op_sel:[0,1,1] op_sel_hi:[1,1,0]
	v_cvt_scalef32_pk_fp8_f16 v137, v140, 1.0 op_sel:[0,0,1]
	v_cvt_scalef32_pk_fp8_f16 v138, v128, 1.0 op_sel:[0,0,1]
	v_mov_b32_e32 v140, v161
	v_mov_b32_e32 v141, v161
	v_mov_b32_e32 v142, v161
	v_mov_b32_e32 v143, v161
	v_mfma_scale_f32_32x32x64_f8f6f4 v[48:63], v[144:151], v[164:171], v[48:63], v227, v226 op_sel_hi:[0,0,0]
	v_mfma_scale_f32_32x32x64_f8f6f4 v[16:31], v[236:243], v[164:171], v[16:31], v227, v226 op_sel_hi:[0,0,0]
	ds_read_b128 v[128:131], v234 offset:40960
	ds_read_b128 v[132:135], v234 offset:41984
	s_waitcnt lgkmcnt(0)
	v_mfma_scale_f32_32x32x64_f8f6f4 v[96:111], v[128:135], v[156:163], v[96:111], v227, v226 op_sel_hi:[0,0,0]
	v_mfma_scale_f32_32x32x64_f8f6f4 v[112:127], v[128:135], v[136:143], v[112:127], v227, v226 op_sel_hi:[0,0,0]
	ds_read_b128 v[128:131], v234 offset:43008
	ds_read_b128 v[132:135], v234 offset:44032
	s_waitcnt lgkmcnt(0)
	v_mfma_scale_f32_32x32x64_f8f6f4 v[64:79], v[128:135], v[156:163], v[64:79], v227, v226 op_sel_hi:[0,0,0]
	v_mfma_scale_f32_32x32x64_f8f6f4 v[80:95], v[128:135], v[136:143], v[80:95], v227, v226 op_sel_hi:[0,0,0]
	ds_read_b128 v[128:131], v234 offset:45056
	ds_read_b128 v[132:135], v234 offset:46080
	s_waitcnt lgkmcnt(0)
	v_mfma_scale_f32_32x32x64_f8f6f4 v[32:47], v[128:135], v[156:163], v[32:47], v227, v226 op_sel_hi:[0,0,0]
	v_mfma_scale_f32_32x32x64_f8f6f4 v[48:63], v[128:135], v[136:143], v[48:63], v227, v226 op_sel_hi:[0,0,0]
	ds_read_b128 v[128:131], v234 offset:47104
	ds_read_b128 v[132:135], v234 offset:48128
	ds_read_b128 v[174:177], v234 offset:49152
	ds_read_b128 v[208:211], v234 offset:50176
	ds_read_b128 v[212:215], v234 offset:53248
	ds_read_b128 v[236:239], v234 offset:54272
	s_waitcnt lgkmcnt(4)
	v_mfma_scale_f32_32x32x64_f8f6f4 v[0:15], v[128:135], v[156:163], v[0:15], v227, v226 op_sel_hi:[0,0,0]
	v_mfma_scale_f32_32x32x64_f8f6f4 v[16:31], v[128:135], v[136:143], v[16:31], v227, v226 op_sel_hi:[0,0,0]
	v_cvt_pk_bf16_f32 v162, v96, v97 clamp
	v_cvt_pk_bf16_f32 v163, v98, v99 clamp
	v_cvt_pk_bf16_f32 v164, v100, v101 clamp
	v_cvt_pk_bf16_f32 v165, v102, v103 clamp
	v_cvt_pk_bf16_f32 v166, v112, v113 clamp
	v_cvt_pk_bf16_f32 v167, v114, v115 clamp
	v_cvt_pk_bf16_f32 v168, v116, v117 clamp
	v_cvt_pk_bf16_f32 v169, v118, v119 clamp
	v_cvt_pk_bf16_f32 v170, v104, v105 clamp
	v_cvt_pk_bf16_f32 v171, v106, v107 clamp
	v_cvt_pk_bf16_f32 v172, v108, v109 clamp
	v_add_u32_e32 v128, 0, v206
	v_cvt_pk_bf16_f32 v173, v110, v111 clamp
	v_add_u32_e32 v235, 0x18000, v128
	v_cvt_pk_bf16_f32 v202, v120, v121 clamp
	ds_read_b128 v[128:131], v235
	ds_read_b128 v[132:135], v235 offset:32
	ds_read_b128 v[136:139], v235 offset:64
	ds_read_b128 v[140:143], v235 offset:96
	v_cvt_pk_bf16_f32 v203, v122, v123 clamp
	ds_read_b128 v[96:99], v235 offset:128
	ds_read_b128 v[100:103], v235 offset:160
	ds_read_b128 v[104:107], v235 offset:192
	ds_read_b128 v[108:111], v235 offset:224
	v_cvt_pk_bf16_f32 v204, v124, v125 clamp
	v_cvt_pk_bf16_f32 v64, v64, v65
	s_waitcnt lgkmcnt(4)
	v_mfma_f32_32x32x16_bf16 v[144:159], v[174:177], v[166:169], v[128:143]
	v_cvt_pk_bf16_f32 v205, v126, v127 clamp
	ds_read_b128 v[240:243], v234 offset:57344
	ds_read_b128 v[244:247], v234 offset:58368
	ds_read_b128 v[248:251], v234 offset:61440
	ds_read_b128 v[252:255], v234 offset:62464
	v_cvt_pk_bf16_f32 v65, v74, v75 clamp
	v_cndmask_b32_e64 v230, v230, 0, s[14:15]
	v_mfma_f32_32x32x16_bf16 v[128:143], v[174:177], v[162:165], v[128:143]
	v_pk_max_i16 v174, v64, 0
	v_cvt_pk_bf16_f32 v175, v66, v67 clamp
	v_cvt_pk_bf16_f32 v176, v68, v69 clamp
	v_cvt_pk_bf16_f32 v177, v70, v71 clamp
	s_waitcnt lgkmcnt(4)
	v_mfma_f32_32x32x16_bf16 v[112:127], v[208:211], v[166:169], v[96:111]
	v_cvt_pk_bf16_f32 v80, v80, v81 clamp
	v_cvt_pk_bf16_f32 v81, v82, v83 clamp
	v_cvt_pk_bf16_f32 v82, v84, v85 clamp
	v_cvt_pk_bf16_f32 v83, v86, v87 clamp
	v_mfma_f32_32x32x16_bf16 v[96:111], v[208:211], v[162:165], v[96:111]
	v_cvt_pk_bf16_f32 v64, v72, v73 clamp
	v_cvt_pk_bf16_f32 v66, v76, v77 clamp
	v_cvt_pk_bf16_f32 v67, v78, v79 clamp
	v_cvt_pk_bf16_f32 v68, v88, v89 clamp
	v_cvt_pk_bf16_f32 v69, v90, v91 clamp
	v_cvt_pk_bf16_f32 v70, v92, v93 clamp
	v_cvt_pk_bf16_f32 v71, v94, v95 clamp
	v_add_u32_e32 v160, 0x14000, v234
	v_mfma_f32_32x32x16_bf16 v[128:143], v[212:215], v[170:173], v[128:143]
	v_mfma_f32_32x32x16_bf16 v[144:159], v[212:215], v[202:205], v[144:159]
	v_mfma_f32_32x32x16_bf16 v[96:111], v[236:239], v[170:173], v[96:111]
	v_mfma_f32_32x32x16_bf16 v[112:127], v[236:239], v[202:205], v[112:127]
	v_cvt_pk_bf16_f32 v76, v32, v33 clamp
	v_cvt_pk_bf16_f32 v77, v34, v35 clamp
	v_cvt_pk_bf16_f32 v78, v36, v37 clamp
	v_cvt_pk_bf16_f32 v79, v38, v39 clamp
	v_cvt_pk_bf16_f32 v88, v48, v49 clamp
	v_cvt_pk_bf16_f32 v89, v50, v51 clamp
	v_cvt_pk_bf16_f32 v90, v52, v53 clamp
	v_cvt_pk_bf16_f32 v91, v54, v55 clamp
	s_waitcnt lgkmcnt(3)
	v_mfma_f32_32x32x16_bf16 v[128:143], v[240:243], v[174:177], v[128:143]
	v_cvt_pk_bf16_f32 v72, v40, v41 clamp
	v_cvt_pk_bf16_f32 v73, v42, v43 clamp
	v_cvt_pk_bf16_f32 v74, v44, v45 clamp
	v_mfma_f32_32x32x16_bf16 v[144:159], v[240:243], v[80:83], v[144:159]
	ds_read_b128 v[92:95], v233 offset:16384
	ds_read_b128 v[208:211], v233 offset:17408
	ds_read_b128 v[236:239], v233 offset:20480
	ds_read_b128 v[240:243], v233 offset:21504
	v_cvt_pk_bf16_f32 v75, v46, v47 clamp
	v_cvt_pk_bf16_f32 v84, v56, v57 clamp
	v_cvt_pk_bf16_f32 v85, v58, v59 clamp
	s_waitcnt lgkmcnt(6)
	v_mfma_f32_32x32x16_bf16 v[96:111], v[244:247], v[174:177], v[96:111]
	v_cvt_pk_bf16_f32 v86, v60, v61 clamp
	v_cvt_pk_bf16_f32 v87, v62, v63 clamp
	v_mfma_f32_32x32x16_bf16 v[112:127], v[244:247], v[80:83], v[112:127]
	s_waitcnt lgkmcnt(5)
	v_mfma_f32_32x32x16_bf16 v[128:143], v[248:251], v[64:67], v[128:143]
	v_mfma_f32_32x32x16_bf16 v[144:159], v[248:251], v[68:71], v[144:159]
	s_waitcnt lgkmcnt(4)
	v_mfma_f32_32x32x16_bf16 v[96:111], v[252:255], v[64:67], v[96:111]
	v_mfma_f32_32x32x16_bf16 v[112:127], v[252:255], v[68:71], v[112:127]
	v_cvt_pk_bf16_f32 v206, v0, v1 clamp
	v_cvt_pk_bf16_f32 v207, v2, v3 clamp
	v_cvt_pk_bf16_f32 v0, v4, v5
	s_waitcnt lgkmcnt(2)
	v_mfma_f32_32x32x16_bf16 v[96:111], v[208:211], v[76:79], v[96:111]
	ds_read_b128 v[32:35], v233 offset:24576
	ds_read_b128 v[36:39], v233 offset:25600
	ds_read_b128 v[40:43], v233 offset:28672
	ds_read_b128 v[44:47], v233 offset:29696
	v_mfma_f32_32x32x16_bf16 v[112:127], v[208:211], v[88:91], v[112:127]
	v_pk_max_i16 v208, v0, 0
	v_cvt_pk_bf16_f32 v209, v6, v7 clamp
	v_cvt_pk_bf16_f32 v214, v16, v17 clamp
	v_cvt_pk_bf16_f32 v215, v18, v19 clamp
	v_cvt_pk_bf16_f32 v216, v20, v21 clamp
	v_cvt_pk_bf16_f32 v217, v22, v23 clamp
	v_mfma_f32_32x32x16_bf16 v[128:143], v[92:95], v[76:79], v[128:143]
	v_cvt_pk_bf16_f32 v0, v8, v9
	v_mfma_f32_32x32x16_bf16 v[144:159], v[92:95], v[88:91], v[144:159]
	v_pk_max_i16 v92, v0, 0
	v_cvt_pk_bf16_f32 v93, v10, v11 clamp
	v_cvt_pk_bf16_f32 v94, v12, v13 clamp
	v_cvt_pk_bf16_f32 v95, v14, v15 clamp
	v_cvt_pk_bf16_f32 v210, v24, v25 clamp
	v_cvt_pk_bf16_f32 v211, v26, v27 clamp
	v_cvt_pk_bf16_f32 v212, v28, v29 clamp
	v_cvt_pk_bf16_f32 v213, v30, v31 clamp
	s_waitcnt lgkmcnt(5)
	v_mfma_f32_32x32x16_bf16 v[128:143], v[236:239], v[72:75], v[128:143]
	v_mfma_f32_32x32x16_bf16 v[144:159], v[236:239], v[84:87], v[144:159]
	s_waitcnt lgkmcnt(4)
	v_mfma_f32_32x32x16_bf16 v[96:111], v[240:243], v[72:75], v[96:111]
	v_mfma_f32_32x32x16_bf16 v[112:127], v[240:243], v[84:87], v[112:127]
	s_waitcnt lgkmcnt(3)
	v_mfma_f32_32x32x16_bf16 v[128:143], v[32:35], v[206:209], v[128:143]
	ds_read_b128 v[0:3], v234 offset:51200
	ds_read_b128 v[236:239], v234 offset:52224
	ds_read_b128 v[240:243], v234 offset:55296
	ds_read_b128 v[244:247], v234 offset:56320
	v_mfma_f32_32x32x16_bf16 v[144:159], v[32:35], v[214:217], v[144:159]
	s_waitcnt lgkmcnt(6)
	v_mfma_f32_32x32x16_bf16 v[96:111], v[36:39], v[206:209], v[96:111]
	v_mfma_f32_32x32x16_bf16 v[112:127], v[36:39], v[214:217], v[112:127]
	s_waitcnt lgkmcnt(5)
	v_mfma_f32_32x32x16_bf16 v[128:143], v[40:43], v[92:95], v[128:143]
	v_mfma_f32_32x32x16_bf16 v[144:159], v[40:43], v[210:213], v[144:159]
	s_waitcnt lgkmcnt(4)
	v_mfma_f32_32x32x16_bf16 v[96:111], v[44:47], v[92:95], v[96:111]
	v_mfma_f32_32x32x16_bf16 v[112:127], v[44:47], v[210:213], v[112:127]
	ds_read_b128 v[32:35], v235 offset:256
	ds_read_b128 v[36:39], v235 offset:288
	ds_read_b128 v[40:43], v235 offset:320
	ds_read_b128 v[44:47], v235 offset:352
	s_nop 3
	v_cvt_pk_bf16_f32 v128, v128, v129 clamp
	v_cvt_pk_bf16_f32 v129, v130, v131 clamp
	v_cvt_pk_bf16_f32 v130, v132, v133 clamp
	v_cvt_pk_bf16_f32 v131, v134, v135 clamp
	s_waitcnt lgkmcnt(0)
	v_mfma_f32_32x32x16_bf16 v[48:63], v[0:3], v[166:169], v[32:47]
	v_cvt_pk_bf16_f32 v132, v144, v145 clamp
	v_cvt_pk_bf16_f32 v133, v146, v147 clamp
	v_cvt_pk_bf16_f32 v134, v148, v149 clamp
	v_cvt_pk_bf16_f32 v135, v150, v151 clamp
	v_mfma_f32_32x32x16_bf16 v[32:47], v[0:3], v[162:165], v[32:47]
	ds_read_b128 v[0:3], v235 offset:384
	ds_read_b128 v[4:7], v235 offset:416
	ds_read_b128 v[8:11], v235 offset:448
	ds_read_b128 v[12:15], v235 offset:480
	s_waitcnt lgkmcnt(0)
	v_mfma_f32_32x32x16_bf16 v[16:31], v[236:239], v[166:169], v[0:15]
	v_mfma_f32_32x32x16_bf16 v[0:15], v[236:239], v[162:165], v[0:15]
	ds_read_b128 v[162:165], v234 offset:59392
	ds_read_b128 v[166:169], v234 offset:60416
	ds_read_b128 v[236:239], v234 offset:63488
	ds_read_b128 v[248:251], v234 offset:64512
	v_mfma_f32_32x32x16_bf16 v[0:15], v[244:247], v[170:173], v[0:15]
	v_mfma_f32_32x32x16_bf16 v[32:47], v[240:243], v[170:173], v[32:47]
	v_mfma_f32_32x32x16_bf16 v[48:63], v[240:243], v[202:205], v[48:63]
	v_mfma_f32_32x32x16_bf16 v[16:31], v[244:247], v[202:205], v[16:31]
	s_waitcnt lgkmcnt(2)
	v_mfma_f32_32x32x16_bf16 v[0:15], v[166:169], v[174:177], v[0:15]
	v_cvt_pk_bf16_f32 v136, v136, v137 clamp
	v_cvt_pk_bf16_f32 v137, v138, v139 clamp
	v_cvt_pk_bf16_f32 v138, v140, v141 clamp
	v_cvt_pk_bf16_f32 v139, v142, v143 clamp
	v_cvt_pk_bf16_f32 v140, v152, v153 clamp
	v_mfma_f32_32x32x16_bf16 v[32:47], v[162:165], v[174:177], v[32:47]
	v_mfma_f32_32x32x16_bf16 v[48:63], v[162:165], v[80:83], v[48:63]
	v_mfma_f32_32x32x16_bf16 v[16:31], v[166:169], v[80:83], v[16:31]
	ds_read_b128 v[80:83], v233 offset:18432
	ds_read_b128 v[144:147], v233 offset:19456
	ds_read_b128 v[148:151], v233 offset:22528
	ds_read_b128 v[162:165], v233 offset:23552
	s_waitcnt lgkmcnt(4)
	v_mfma_f32_32x32x16_bf16 v[0:15], v[248:251], v[64:67], v[0:15]
	v_mfma_f32_32x32x16_bf16 v[32:47], v[236:239], v[64:67], v[32:47]
	v_cvt_pk_bf16_f32 v141, v154, v155 clamp
	v_cvt_pk_bf16_f32 v142, v156, v157 clamp
	v_cvt_pk_bf16_f32 v143, v158, v159 clamp
	v_mfma_f32_32x32x16_bf16 v[48:63], v[236:239], v[68:71], v[48:63]
	v_mfma_f32_32x32x16_bf16 v[16:31], v[248:251], v[68:71], v[16:31]
	s_waitcnt lgkmcnt(2)
	v_mfma_f32_32x32x16_bf16 v[0:15], v[144:147], v[76:79], v[0:15]
	v_mfma_f32_32x32x16_bf16 v[32:47], v[80:83], v[76:79], v[32:47]
	v_mfma_f32_32x32x16_bf16 v[48:63], v[80:83], v[88:91], v[48:63]
	ds_read_b128 v[64:67], v233 offset:26624
	ds_read_b128 v[68:71], v233 offset:27648
	ds_read_b128 v[76:79], v233 offset:30720
	ds_read_b128 v[80:83], v233 offset:31744
	v_mfma_f32_32x32x16_bf16 v[16:31], v[144:147], v[88:91], v[16:31]
	v_cvt_pk_bf16_f32 v96, v96, v97 clamp
	v_cvt_pk_bf16_f32 v97, v98, v99 clamp
	v_cvt_pk_bf16_f32 v98, v100, v101 clamp
	v_cvt_pk_bf16_f32 v99, v102, v103 clamp
	s_waitcnt lgkmcnt(4)
	v_mfma_f32_32x32x16_bf16 v[0:15], v[162:165], v[72:75], v[0:15]
	v_cvt_pk_bf16_f32 v100, v112, v113 clamp
	v_mfma_f32_32x32x16_bf16 v[32:47], v[148:151], v[72:75], v[32:47]
	v_cvt_pk_bf16_f32 v101, v114, v115 clamp
	v_cvt_pk_bf16_f32 v102, v116, v117 clamp
	v_cvt_pk_bf16_f32 v103, v118, v119 clamp
	v_mfma_f32_32x32x16_bf16 v[48:63], v[148:151], v[84:87], v[48:63]
	v_mfma_f32_32x32x16_bf16 v[16:31], v[162:165], v[84:87], v[16:31]
	s_waitcnt lgkmcnt(2)
	v_mfma_f32_32x32x16_bf16 v[0:15], v[68:71], v[206:209], v[0:15]
	ds_read_b128 v[84:87], v160
	ds_read_b128 v[112:115], v160 offset:1024
	ds_read_b128 v[116:119], v160 offset:2048
	ds_read_b128 v[144:147], v160 offset:3072
	v_mfma_f32_32x32x16_bf16 v[32:47], v[64:67], v[206:209], v[32:47]
	v_mfma_f32_32x32x16_bf16 v[48:63], v[64:67], v[214:217], v[48:63]
	v_cvt_pk_bf16_f32 v104, v104, v105 clamp
	v_cvt_pk_bf16_f32 v105, v106, v107 clamp
	v_cvt_pk_bf16_f32 v106, v108, v109 clamp
	v_cvt_pk_bf16_f32 v107, v110, v111 clamp
	v_mfma_f32_32x32x16_bf16 v[16:31], v[68:71], v[214:217], v[16:31]
	v_cvt_pk_bf16_f32 v108, v120, v121 clamp
	v_cvt_pk_bf16_f32 v109, v122, v123 clamp
	v_cvt_pk_bf16_f32 v110, v124, v125 clamp
	s_waitcnt lgkmcnt(4)
	v_mfma_f32_32x32x16_bf16 v[0:15], v[80:83], v[92:95], v[0:15]
	v_cvt_pk_bf16_f32 v111, v126, v127 clamp
	v_mfma_f32_32x32x16_bf16 v[32:47], v[76:79], v[92:95], v[32:47]
	v_mfma_f32_32x32x16_bf16 v[48:63], v[76:79], v[210:213], v[48:63]
	v_mfma_f32_32x32x16_bf16 v[16:31], v[80:83], v[210:213], v[16:31]
	s_waitcnt lgkmcnt(3)
	v_mfma_f32_4x4x4_16b_bf16 v[64:67], v[84:85], v[128:129], 0
	v_mfma_f32_4x4x4_16b_bf16 v[68:71], v[86:87], v[130:131], 0
	s_nop 7
	v_cvt_pk_bf16_f32 v32, v32, v33 clamp
	v_cvt_pk_bf16_f32 v33, v34, v35 clamp
	v_cvt_pk_bf16_f32 v34, v36, v37 clamp
	v_cvt_pk_bf16_f32 v35, v38, v39 clamp
	v_mfma_f32_4x4x4_16b_bf16 v[80:83], v[84:85], v[132:133], 0
	v_mfma_f32_4x4x4_16b_bf16 v[88:91], v[86:87], v[134:135], 0
	v_cvt_pk_bf16_f32 v48, v48, v49 clamp
	v_cvt_pk_bf16_f32 v49, v50, v51 clamp
	v_cvt_pk_bf16_f32 v50, v52, v53 clamp
	v_cvt_pk_bf16_f32 v51, v54, v55 clamp
	s_waitcnt lgkmcnt(2)
	v_mfma_f32_4x4x4_16b_bf16 v[64:67], v[112:113], v[136:137], v[64:67]
	v_mfma_f32_4x4x4_16b_bf16 v[68:71], v[114:115], v[138:139], v[68:71]
	v_cvt_pk_bf16_f32 v40, v40, v41 clamp
	v_cvt_pk_bf16_f32 v41, v42, v43 clamp
	v_cvt_pk_bf16_f32 v42, v44, v45 clamp
	v_cvt_pk_bf16_f32 v43, v46, v47 clamp
	v_mfma_f32_4x4x4_16b_bf16 v[80:83], v[112:113], v[140:141], v[80:83]
	v_mfma_f32_4x4x4_16b_bf16 v[88:91], v[114:115], v[142:143], v[88:91]
	v_cvt_pk_bf16_f32 v52, v56, v57
	v_cvt_pk_bf16_f32 v53, v58, v59
	v_cvt_pk_bf16_f32 v54, v60, v61
	v_cvt_pk_bf16_f32 v55, v62, v63
	s_waitcnt lgkmcnt(1)
	v_mfma_f32_4x4x4_16b_bf16 v[64:67], v[116:117], v[96:97], v[64:67]
	v_mfma_f32_4x4x4_16b_bf16 v[68:71], v[118:119], v[98:99], v[68:71]
	ds_read_b128 v[36:39], v160 offset:4096
	ds_read_b128 v[96:99], v160 offset:5120
	v_cvt_pk_bf16_f32 v0, v0, v1 clamp
	v_cvt_pk_bf16_f32 v1, v2, v3 clamp
	v_cvt_pk_bf16_f32 v2, v4, v5 clamp
	v_cvt_pk_bf16_f32 v3, v6, v7 clamp
	v_mfma_f32_4x4x4_16b_bf16 v[80:83], v[116:117], v[100:101], v[80:83]
	v_mfma_f32_4x4x4_16b_bf16 v[88:91], v[118:119], v[102:103], v[88:91]
	ds_read_b128 v[4:7], v160 offset:7168
	v_cvt_pk_bf16_f32 v12, v12, v13
	v_cvt_pk_bf16_f32 v13, v14, v15
	v_cvt_pk_bf16_f32 v24, v24, v25
	v_cvt_pk_bf16_f32 v25, v26, v27
	s_waitcnt lgkmcnt(3)
	v_mfma_f32_4x4x4_16b_bf16 v[64:67], v[144:145], v[104:105], v[64:67]
	v_mfma_f32_4x4x4_16b_bf16 v[68:71], v[146:147], v[106:107], v[68:71]
	v_cvt_pk_bf16_f32 v26, v28, v29
	v_cvt_pk_bf16_f32 v27, v30, v31
	v_cndmask_b32_e64 v219, v219, 0, s[14:15]
	v_cndmask_b32_e64 v218, v218, 0, s[14:15]
	v_mfma_f32_4x4x4_16b_bf16 v[80:83], v[144:145], v[108:109], v[80:83]
	v_mfma_f32_4x4x4_16b_bf16 v[88:91], v[146:147], v[110:111], v[88:91]
	s_waitcnt lgkmcnt(2)
	v_mfma_f32_4x4x4_16b_bf16 v[64:67], v[36:37], v[32:33], v[64:67]
	v_mfma_f32_4x4x4_16b_bf16 v[68:71], v[38:39], v[34:35], v[68:71]
	v_cvt_pk_bf16_f32 v34, v20, v21
	v_cvt_pk_bf16_f32 v35, v22, v23
	ds_read_b128 v[20:23], v160 offset:6144
	v_cvt_pk_bf16_f32 v32, v16, v17
	v_cvt_pk_bf16_f32 v33, v18, v19
	v_pk_max_i16 v16, v52, 0
	v_pk_max_i16 v17, v53, 0
	v_mfma_f32_4x4x4_16b_bf16 v[80:83], v[36:37], v[48:49], v[80:83]
	v_mfma_f32_4x4x4_16b_bf16 v[88:91], v[38:39], v[50:51], v[88:91]
	v_pk_max_i16 v18, v54, 0
	v_pk_max_i16 v19, v55, 0
	s_waitcnt lgkmcnt(2)
	v_mfma_f32_4x4x4_16b_bf16 v[64:67], v[96:97], v[40:41], v[64:67]
	v_mfma_f32_4x4x4_16b_bf16 v[68:71], v[98:99], v[42:43], v[68:71]
	v_mfma_f32_4x4x4_16b_bf16 v[80:83], v[96:97], v[16:17], v[80:83]
	v_mfma_f32_4x4x4_16b_bf16 v[88:91], v[98:99], v[18:19], v[88:91]
	v_cvt_pk_bf16_f32 v16, v8, v9
	v_cvt_pk_bf16_f32 v17, v10, v11
	v_pk_max_i16 v8, v24, 0
	v_pk_max_i16 v9, v25, 0
	v_pk_max_i16 v10, v26, 0
	v_pk_max_i16 v11, v27, 0
	s_waitcnt lgkmcnt(0)
	v_mfma_f32_4x4x4_16b_bf16 v[64:67], v[20:21], v[0:1], v[64:67]
	v_mfma_f32_4x4x4_16b_bf16 v[68:71], v[22:23], v[2:3], v[68:71]
	v_pk_max_i16 v0, v32, 0
	v_pk_max_i16 v1, v33, 0
	v_pk_max_i16 v2, v34, 0
	v_pk_max_i16 v3, v35, 0
	s_nop 1
	v_mfma_f32_4x4x4_16b_bf16 v[80:83], v[20:21], v[0:1], v[80:83]
	v_mfma_f32_4x4x4_16b_bf16 v[88:91], v[22:23], v[2:3], v[88:91]
	v_pk_max_i16 v0, v16, 0
	v_pk_max_i16 v1, v17, 0
	v_pk_max_i16 v2, v12, 0
	v_pk_max_i16 v3, v13, 0
	s_nop 1
	v_mfma_f32_4x4x4_16b_bf16 v[64:67], v[4:5], v[0:1], v[64:67]
	v_mfma_f32_4x4x4_16b_bf16 v[68:71], v[6:7], v[2:3], v[68:71]
	v_mfma_f32_4x4x4_16b_bf16 v[80:83], v[4:5], v[8:9], v[80:83]
	v_mfma_f32_4x4x4_16b_bf16 v[88:91], v[6:7], v[10:11], v[88:91]
	s_waitcnt vmcnt(10)
	s_nop 3
	v_pk_add_f32 v[64:65], v[64:65], v[68:69]
	v_pk_add_f32 v[80:81], v[80:81], v[88:89]
	v_add_f32_e32 v66, v66, v70
	v_add_f32_e32 v82, v82, v90
	s_nop 1
	v_permlane32_swap_b32_e32 v64, v80
	v_permlane32_swap_b32_e32 v65, v81
	v_permlane32_swap_b32_e32 v66, v82
	s_nop 0
	v_add_f32_e32 v64, v64, v80
	v_add_f32_e32 v65, v65, v81
	v_add_f32_e32 v66, v66, v82
	v_add_f32_e32 v3, s10, v64
	v_add_f32_e32 v4, s11, v65
	v_add_f32_e32 v5, s18, v66
	v_mul_f32_e32 v3, 0xbfb8aa3b, v3
	v_mul_f32_e32 v4, 0xbfb8aa3b, v4
	v_mul_f32_e32 v5, 0xbfb8aa3b, v5
	v_exp_f32_e32 v3, v3
	v_exp_f32_e32 v4, v4
	v_exp_f32_e32 v5, v5
	v_add_f32_e32 v3, 1.0, v3
	v_add_f32_e32 v4, 1.0, v4
	v_add_f32_e32 v5, 1.0, v5
	v_rcp_f32_e32 v3, v3
	v_rcp_f32_e32 v4, v4
	v_rcp_f32_e32 v5, v5
	v_fmac_f32_e32 v218, v232, v3
	v_fmac_f32_e32 v219, v232, v4
	v_fmac_f32_e32 v230, v232, v5
	s_andn2_b64 vcc, exec, s[12:13]
	s_cbranch_vccnz .LBB1_6
	v_add_f32_dpp v218, v218, v218 row_shr:1 row_mask:0xf bank_mask:0xf bound_ctrl:1
	v_add_f32_dpp v219, v219, v219 row_shr:1 row_mask:0xf bank_mask:0xf bound_ctrl:1
	v_add_f32_dpp v230, v230, v230 row_shr:1 row_mask:0xf bank_mask:0xf bound_ctrl:1
	v_add_f32_dpp v218, v218, v218 row_shr:2 row_mask:0xf bank_mask:0xf bound_ctrl:1
	v_add_f32_dpp v219, v219, v219 row_shr:2 row_mask:0xf bank_mask:0xf bound_ctrl:1
	v_add_f32_dpp v230, v230, v230 row_shr:2 row_mask:0xf bank_mask:0xf bound_ctrl:1
	v_add_f32_dpp v218, v218, v218 row_shr:4 row_mask:0xf bank_mask:0xf bound_ctrl:1
	v_add_f32_dpp v219, v219, v219 row_shr:4 row_mask:0xf bank_mask:0xf bound_ctrl:1
	v_add_f32_dpp v230, v230, v230 row_shr:4 row_mask:0xf bank_mask:0xf bound_ctrl:1
	v_add_f32_dpp v218, v218, v218 row_shr:8 row_mask:0xf bank_mask:0xf bound_ctrl:1
	v_add_f32_dpp v219, v219, v219 row_shr:8 row_mask:0xf bank_mask:0xf bound_ctrl:1
	v_add_f32_dpp v230, v230, v230 row_shr:8 row_mask:0xf bank_mask:0xf bound_ctrl:1
	v_mov_b32_e32 v0, 0
	v_mov_b32_e32 v1, 0
	v_mov_b32_e32 v5, 0
	v_mov_b32_dpp v0, v218 row_bcast:15 row_mask:0xa bank_mask:0xf
	v_mov_b32_dpp v1, v219 row_bcast:15 row_mask:0xa bank_mask:0xf
	v_mov_b32_dpp v5, v230 row_bcast:15 row_mask:0xa bank_mask:0xf
	v_lshl_add_u32 v6, v231, 1, v231
	v_ashrrev_i32_e32 v7, 31, v6
	v_add_f32_e32 v218, v218, v0
	v_add_f32_e32 v219, v219, v1
	v_add_f32_e32 v230, v230, v5
	v_mov_b32_e32 v0, 0
	v_mov_b32_e32 v1, 0
	v_mov_b32_e32 v5, 0
	v_mov_b32_dpp v0, v218 row_bcast:31 row_mask:0xc bank_mask:0xf
	v_mov_b32_dpp v1, v219 row_bcast:31 row_mask:0xc bank_mask:0xf
	v_mov_b32_dpp v5, v230 row_bcast:31 row_mask:0xc bank_mask:0xf
	v_lshl_add_u64 v[6:7], v[6:7], 2, s[8:9]
	v_cmp_eq_u32_e32 vcc, 63, v220
	v_add_f32_e32 v2, v218, v0
	v_add_f32_e32 v3, v219, v1
	v_add_f32_e32 v4, v230, v5
	s_and_saveexec_b64 s[12:13], vcc
	global_store_dwordx3 v[6:7], v[2:4], off
	s_branch .LBB1_5
